# speedup vs baseline: 1.0116x; 1.0116x over previous
.LBB2_13:
	v_exp_f32_e32 v48, v48
	v_exp_f32_e32 v49, v49
	v_mfma_f32_32x32x16_bf16 v[112:127], a[192:195], a[128:131], v[16:31]
	ds_read_b64_tr_b16 v[180:181], v223 offset:0
	v_cvt_pk_bf16_f32 v164, v128, v129
	v_exp_f32_e32 v50, v50
	v_exp_f32_e32 v51, v51
	v_mfma_f32_32x32x16_bf16 v[96:111], a[192:195], a[160:163], v[0:15]
	ds_read_b64_tr_b16 v[182:183], v223 offset:0x800
	v_cvt_pk_bf16_f32 v165, v130, v131
	v_mfma_f32_32x32x16_bf16 v[80:95], a[224:227], a[128:131], v[16:31]
	ds_read_b64_tr_b16 v[184:185], v223 offset:0x200
	v_exp_f32_e32 v236, v52
	v_exp_f32_e32 v237, v53
	v_cvt_pk_bf16_f32 v166, v132, v133
	v_mfma_f32_32x32x16_bf16 v[64:79], a[224:227], a[160:163], v[0:15]
	ds_read_b64_tr_b16 v[186:187], v223 offset:0xa00
	ds_read_b64_tr_b16 v[176:177], v223 offset:0x400
	v_exp_f32_e32 v242, v54
	v_exp_f32_e32 v243, v55
	v_cvt_pk_bf16_f32 v167, v134, v135
	v_exp_f32_e32 v198, v56
	v_exp_f32_e32 v199, v57
	v_mfma_f32_32x32x16_bf16 v[112:127], a[196:199], a[132:135], v[112:127]
	ds_read_b64_tr_b16 v[178:179], v223 offset:0xc00
	v_cvt_pk_bf16_f32 v128, v136, v137
	v_exp_f32_e32 v230, v58
	v_exp_f32_e32 v231, v59
	v_mfma_f32_32x32x16_bf16 v[96:111], a[196:199], a[164:167], v[96:111]
	ds_read_b64_tr_b16 v[188:189], v223 offset:0x600
	v_cvt_pk_bf16_f32 v129, v138, v139
	v_exp_f32_e32 v232, v60
	v_exp_f32_e32 v233, v61
	v_mfma_f32_32x32x16_bf16 v[80:95], a[228:231], a[132:135], v[80:95]
	ds_read_b64_tr_b16 v[190:191], v223 offset:0xe00
	v_cvt_pk_bf16_f32 v130, v140, v141
	v_mfma_f32_32x32x16_bf16 v[64:79], a[228:231], a[164:167], v[64:79]
	ds_read_b64_tr_b16 v[172:173], v223 offset:0x1000
	v_exp_f32_e32 v234, v62
	v_exp_f32_e32 v235, v63
	ds_read_b64_tr_b16 v[174:175], v223 offset:0x1800
	v_cvt_pk_bf16_f32 v131, v142, v143
	v_exp_f32_e32 v141, v32
	v_exp_f32_e32 v142, v33
	v_mfma_f32_32x32x16_bf16 v[112:127], a[200:203], a[136:139], v[112:127]
	ds_read_b64_tr_b16 v[168:169], v223 offset:0x1200
	v_cvt_pk_bf16_f32 v192, v144, v145
	v_exp_f32_e32 v143, v34
	v_mfma_f32_32x32x16_bf16 v[96:111], a[200:203], a[168:171], v[96:111]
	ds_read_b64_tr_b16 v[170:171], v223 offset:0x1a00
	v_exp_f32_e32 v244, v35
	v_cvt_pk_bf16_f32 v193, v146, v147
	v_mfma_f32_32x32x16_bf16 v[80:95], a[232:235], a[136:139], v[80:95]
	ds_read_b64_tr_b16 v[160:161], v223 offset:0x1400
	v_exp_f32_e32 v245, v36
	v_exp_f32_e32 v246, v37
	v_cvt_pk_bf16_f32 v194, v148, v149
	v_mfma_f32_32x32x16_bf16 v[64:79], a[232:235], a[168:171], v[64:79]
	ds_read_b64_tr_b16 v[162:163], v223 offset:0x1c00
	ds_read_b64_tr_b16 v[136:137], v223 offset:0x1600
	v_exp_f32_e32 v247, v38
	v_exp_f32_e32 v248, v39
	v_cvt_pk_bf16_f32 v195, v150, v151
	v_exp_f32_e32 v148, v40
	v_exp_f32_e32 v149, v41
	v_mfma_f32_32x32x16_bf16 v[112:127], a[204:207], a[140:143], v[112:127]
	ds_read_b64_tr_b16 v[138:139], v223 offset:0x1e00
	v_cvt_pk_bf16_f32 v144, v152, v153
	v_exp_f32_e32 v150, v42
	v_exp_f32_e32 v151, v43
	v_mfma_f32_32x32x16_bf16 v[96:111], a[204:207], a[172:175], v[96:111]
	ds_read_b64_tr_b16 v[132:133], v223 offset:0x2000
	v_cvt_pk_bf16_f32 v145, v154, v155
	v_exp_f32_e32 v152, v44
	v_exp_f32_e32 v153, v45
	v_mfma_f32_32x32x16_bf16 v[80:95], a[236:239], a[140:143], v[80:95]
	ds_read_b64_tr_b16 v[134:135], v223 offset:0x2800
	v_cvt_pk_bf16_f32 v146, v156, v157
	v_mfma_f32_32x32x16_bf16 v[64:79], a[236:239], a[172:175], v[64:79]
	ds_read_b64_tr_b16 v[60:61], v223 offset:0x2200
	v_exp_f32_e32 v154, v46
	v_exp_f32_e32 v155, v47
	ds_read_b64_tr_b16 v[62:63], v223 offset:0x2a00
	v_cvt_pk_bf16_f32 v147, v158, v159
	s_mov_b32 s0, s30
	v_mfma_f32_32x32x16_bf16 v[112:127], a[208:211], a[144:147], v[112:127]
	ds_read_b64_tr_b16 v[56:57], v223 offset:0x2400
	v_cvt_pk_bf16_f32 v52, v48, v49
	v_add_f32_e32 v32, v239, v48
	v_add_f32_e32 v33, v238, v49
	s_add_i32 s19, s17, 0xfffda000
	s_mov_b32 s1, s19
	v_mfma_f32_32x32x16_bf16 v[96:111], a[208:211], a[176:179], v[96:111]
	ds_read_b64_tr_b16 v[58:59], v223 offset:0x2c00
	v_cvt_pk_bf16_f32 v53, v50, v51
	v_add_f32_e32 v32, v32, v50
	v_add_f32_e32 v33, v33, v51
	s_mov_b32 s81, s37
	v_mfma_f32_32x32x16_bf16 v[80:95], a[240:243], a[144:147], v[80:95]
	ds_read_b64_tr_b16 v[48:49], v223 offset:0x2600
	v_cvt_pk_bf16_f32 v54, v236, v237
	v_add_f32_e32 v32, v32, v236
	v_add_f32_e32 v33, v33, v237
	s_add_i32 s82, s17, 0xfffdc000
	v_mfma_f32_32x32x16_bf16 v[64:79], a[240:243], a[176:179], v[64:79]
	ds_read_b64_tr_b16 v[50:51], v223 offset:0x2e00
	ds_read_b64_tr_b16 v[44:45], v223 offset:0x3000
	v_cvt_pk_bf16_f32 v55, v242, v243
	v_add_f32_e32 v32, v32, v242
	v_add_f32_e32 v33, v33, v243
	s_mov_b32 s83, s39
	v_mfma_f32_32x32x16_bf16 v[112:127], a[212:215], a[148:151], v[112:127]
	ds_read_b64_tr_b16 v[46:47], v223 offset:0x3800
	v_add_f32_e32 v32, v32, v198
	v_add_f32_e32 v33, v33, v199
	s_add_i32 s24, s17, 0xfffde000
	s_mov_b32 s84, s24
	v_mfma_f32_32x32x16_bf16 v[96:111], a[212:215], a[180:183], v[96:111]
	ds_read_b64_tr_b16 v[40:41], v223 offset:0x3200
	v_add_f32_e32 v32, v32, v230
	v_add_f32_e32 v33, v33, v231
	s_mov_b32 s85, s41
	v_mfma_f32_32x32x16_bf16 v[80:95], a[244:247], a[148:151], v[80:95]
	ds_read_b64_tr_b16 v[42:43], v223 offset:0x3a00
	v_add_f32_e32 v32, v32, v232
	v_add_f32_e32 v33, v33, v233
	s_add_i32 s86, s17, 0xfffe0000
	v_mfma_f32_32x32x16_bf16 v[64:79], a[244:247], a[180:183], v[64:79]
	ds_read_b64_tr_b16 v[36:37], v223 offset:0x3400
	ds_read_b64_tr_b16 v[38:39], v223 offset:0x3c00
	v_add_f32_e32 v156, v32, v234
	v_add_f32_e32 v157, v33, v235
	s_mov_b32 s87, s43
	v_mfma_f32_32x32x16_bf16 v[112:127], a[216:219], a[152:155], v[112:127]
	ds_read_b64_tr_b16 v[32:33], v223 offset:0x3600
	v_cvt_pk_bf16_f32 v140, v141, v142
	v_add_f32_e32 v158, v240, v141
	v_add_f32_e32 v142, v241, v142
	s_add_i32 s88, s17, 0xfffba000
	v_mfma_f32_32x32x16_bf16 v[96:111], a[216:219], a[184:187], v[96:111]
	ds_read_b64_tr_b16 v[34:35], v223 offset:0x3e00
	v_cvt_pk_bf16_f32 v141, v143, v244
	v_add_f32_e32 v143, v158, v143
	v_add_f32_e32 v158, v142, v244
	v_mfma_f32_32x32x16_bf16 v[80:95], a[248:251], a[152:155], v[80:95]
	s_mov_b32 s89, s45
	v_cvt_pk_bf16_f32 v142, v245, v246
	v_add_f32_e32 v159, v143, v245
	v_add_f32_e32 v158, v158, v246
	v_mfma_f32_32x32x16_bf16 v[64:79], a[248:251], a[184:187], v[64:79]
	s_add_i32 s90, s17, 0xfffba080
	v_cvt_pk_bf16_f32 v143, v247, v248
	v_add_f32_e32 v159, v159, v247
	v_add_f32_e32 v158, v158, v248
	v_mfma_f32_32x32x16_bf16 v[112:127], a[220:223], a[156:159], v[112:127]
	s_mov_b32 s91, s47
	v_add_f32_e32 v159, v159, v148
	v_add_f32_e32 v158, v158, v149
	v_mfma_f32_32x32x16_bf16 v[96:111], a[220:223], a[188:191], v[96:111]
	s_add_i32 s92, s17, 0xfffbe000
	v_add_f32_e32 v159, v159, v150
	v_add_f32_e32 v158, v158, v151
	v_mfma_f32_32x32x16_bf16 v[80:95], a[252:255], a[156:159], v[80:95]
	s_mov_b32 s93, s49
	v_add_f32_e32 v159, v159, v152
	v_add_f32_e32 v158, v158, v153
	v_mfma_f32_32x32x16_bf16 v[64:79], a[252:255], a[188:191], v[64:79]
	s_add_i32 s94, s17, 0xfffbe080
	v_add_f32_e32 v159, v159, v154
	v_add_f32_e32 v158, v158, v155
	s_nop 4
	v_add_f32_e32 v156, v156, v157
	s_waitcnt vmcnt(0) lgkmcnt(0)
	s_barrier
	s_nop 0
	v_mov_b32_e32 v157, v156
	s_nop 1
	v_permlane32_swap_b32_e32 v156, v157
	v_add_f32_e32 v156, v156, v157
	v_add_f32_e32 v197, v197, v156
	v_add_f32_e32 v156, v159, v158
	v_mov_b32_e32 v157, v156
	s_nop 1
	v_permlane32_swap_b32_e32 v156, v157
	v_add_f32_e32 v156, v156, v157
	v_add_f32_e32 v196, v196, v156
	s_nop 1
	v_mfma_f32_32x32x16_bf16 a[0:15], v[180:183], v[164:167], a[0:15]
	s_mov_b32 m0, s0
	s_nop 0
	buffer_load_dwordx4 v209, s[4:7], s1 offen lds
	v_mfma_f32_32x32x16_bf16 a[16:31], v[180:183], v[192:195], a[16:31]
	s_mov_b32 m0, s81
	s_nop 0
	buffer_load_dwordx4 v210, s[4:7], s82 offen lds
	ds_read_b128 a[192:195], v219 offset:0
	v_mfma_f32_32x32x16_bf16 a[32:47], v[184:187], v[164:167], a[32:47]
	s_mov_b32 m0, s83
	s_nop 0
	buffer_load_dwordx4 v209, s[4:7], s84 offen lds
	ds_read_b128 a[196:199], v220 offset:0
	v_mfma_f32_32x32x16_bf16 a[48:63], v[184:187], v[192:195], a[48:63]
	s_mov_b32 m0, s85
	s_nop 0
	buffer_load_dwordx4 v210, s[4:7], s86 offen lds
	ds_read_b128 a[200:203], v221 offset:0
	v_mfma_f32_32x32x16_bf16 a[64:79], v[176:179], v[164:167], a[64:79]
	s_mov_b32 m0, s87
	s_nop 0
	buffer_load_dwordx4 v211, s[20:23], s88 offen lds
	ds_read_b128 a[204:207], v222 offset:0
	v_mfma_f32_32x32x16_bf16 a[80:95], v[176:179], v[192:195], a[80:95]
	s_mov_b32 m0, s89
	s_nop 0
	buffer_load_dwordx4 v211, s[20:23], s90 offen lds
	ds_read_b128 a[208:211], v219 offset:128
	v_mfma_f32_32x32x16_bf16 a[96:111], v[188:191], v[164:167], a[96:111]
	s_mov_b32 m0, s91
	s_nop 0
	buffer_load_dwordx4 v211, s[20:23], s92 offen lds
	ds_read_b128 a[212:215], v220 offset:128
	v_mfma_f32_32x32x16_bf16 a[112:127], v[188:191], v[192:195], a[112:127]
	s_mov_b32 m0, s93
	s_nop 0
	buffer_load_dwordx4 v211, s[20:23], s94 offen lds
	ds_read_b128 a[216:219], v221 offset:128
	v_mfma_f32_32x32x16_bf16 a[0:15], v[172:175], v[128:131], a[0:15]
	ds_read_b128 a[220:223], v222 offset:128
	v_max3_f32 v156, v112, v113, v80
	v_max3_f32 v157, v114, v115, v81
	v_max3_f32 v156, v156, v82, v83
	v_mfma_f32_32x32x16_bf16 a[16:31], v[172:175], v[144:147], a[16:31]
	ds_read_b128 a[224:227], v219 offset:8192
	v_max3_f32 v156, v156, v116, v117
	v_max3_f32 v157, v157, v118, v119
	v_max3_f32 v156, v156, v84, v85
	v_max3_f32 v157, v157, v86, v87
	v_mfma_f32_32x32x16_bf16 a[32:47], v[168:171], v[128:131], a[32:47]
	ds_read_b128 a[228:231], v220 offset:8192
	v_max3_f32 v156, v156, v120, v121
	v_max3_f32 v157, v157, v122, v123
	v_max3_f32 v156, v156, v88, v89
	v_max3_f32 v157, v157, v90, v91
	v_mfma_f32_32x32x16_bf16 a[48:63], v[168:171], v[144:147], a[48:63]
	ds_read_b128 a[232:235], v221 offset:8192
	v_max3_f32 v156, v156, v124, v125
	v_max3_f32 v157, v157, v126, v127
	v_max3_f32 v156, v156, v92, v93
	v_max3_f32 v157, v157, v94, v95
	v_mfma_f32_32x32x16_bf16 a[64:79], v[160:163], v[128:131], a[64:79]
	ds_read_b128 a[236:239], v222 offset:8192
	v_max3_f32 v158, v96, v97, v64
	v_max3_f32 v159, v98, v99, v65
	v_max3_f32 v158, v158, v66, v67
	v_mfma_f32_32x32x16_bf16 a[80:95], v[160:163], v[144:147], a[80:95]
	ds_read_b128 a[240:243], v219 offset:8320
	v_max3_f32 v158, v158, v100, v101
	v_max3_f32 v159, v159, v102, v103
	v_max3_f32 v158, v158, v68, v69
	v_max3_f32 v159, v159, v70, v71
	v_mfma_f32_32x32x16_bf16 a[96:111], v[136:139], v[128:131], a[96:111]
	ds_read_b128 a[244:247], v220 offset:8320
	v_max3_f32 v128, v158, v104, v105
	v_max3_f32 v129, v159, v106, v107
	v_max3_f32 v128, v128, v72, v73
	v_max3_f32 v129, v129, v74, v75
	v_mfma_f32_32x32x16_bf16 a[112:127], v[136:139], v[144:147], a[112:127]
	ds_read_b128 a[248:251], v221 offset:8320
	v_max3_f32 v128, v128, v108, v109
	v_max3_f32 v129, v129, v110, v111
	v_max3_f32 v128, v128, v76, v77
	v_max3_f32 v130, v129, v78, v79
	v_mfma_f32_32x32x16_bf16 a[0:15], v[132:135], v[52:55], a[0:15]
	ds_read_b128 a[252:255], v222 offset:8320
	v_max_f32_e32 v129, v156, v157
	v_mov_b32_e32 v131, v129
	s_nop 1
	v_permlane32_swap_b32_e32 v129, v131
	v_max_f32_e32 v129, v129, v131
	v_mfma_f32_32x32x16_bf16 a[16:31], v[132:135], v[140:143], a[16:31]
	v_max_f32_e32 v128, v128, v130
	v_mov_b32_e32 v130, v128
	s_nop 1
	v_permlane32_swap_b32_e32 v128, v130
	v_max_f32_e32 v128, v128, v130
	v_max_f32_e32 v130, v129, v129
	v_max_f32_e32 v131, v128, v128
	v_max_f32_e32 v130, v130, v131
	v_mfma_f32_32x32x16_bf16 a[32:47], v[60:63], v[52:55], a[32:47]
	v_cmp_lt_f32_e32 vcc, s79, v130
	s_cmp_lg_u64 vcc, 0
	s_cselect_b64 s[0:1], -1, 0
	s_cbranch_vccnz .LBB2_18
.LBB2_14:
	v_cvt_pk_bf16_f32 v156, v198, v199
	v_cvt_pk_bf16_f32 v157, v230, v231
	v_cvt_pk_bf16_f32 v158, v232, v233
	v_cvt_pk_bf16_f32 v159, v234, v235
	v_cvt_pk_bf16_f32 v160, v148, v149
	v_cvt_pk_bf16_f32 v161, v150, v151
	v_cvt_pk_bf16_f32 v162, v152, v153
	v_cvt_pk_bf16_f32 v163, v154, v155
	v_exp_f32_e32 v128, v112
	v_exp_f32_e32 v129, v113
	v_mfma_f32_32x32x16_bf16 a[48:63], v[60:63], v[140:143], a[48:63]
	v_exp_f32_e32 v130, v114
	v_exp_f32_e32 v131, v115
	v_mfma_f32_32x32x16_bf16 a[64:79], v[56:59], v[52:55], a[64:79]
	v_add_f32_e32 v60, v201, v128
	v_add_f32_e32 v61, v201, v129
	v_exp_f32_e32 v132, v116
	v_exp_f32_e32 v133, v117
	v_exp_f32_e32 v134, v118
	v_mfma_f32_32x32x16_bf16 a[80:95], v[56:59], v[140:143], a[80:95]
	v_add_f32_e32 v56, v60, v130
	v_add_f32_e32 v57, v61, v131
	v_exp_f32_e32 v135, v119
	v_exp_f32_e32 v136, v120
	v_mfma_f32_32x32x16_bf16 a[96:111], v[48:51], v[52:55], a[96:111]
	v_add_f32_e32 v52, v56, v132
	v_add_f32_e32 v53, v57, v133
	v_add_f32_e32 v52, v52, v134
	v_exp_f32_e32 v137, v121
	v_exp_f32_e32 v138, v122
	v_exp_f32_e32 v139, v123
	v_mfma_f32_32x32x16_bf16 a[112:127], v[48:51], v[140:143], a[112:127]
	v_add_f32_e32 v48, v53, v135
	v_add_f32_e32 v49, v52, v136
	v_exp_f32_e32 v140, v124
	v_exp_f32_e32 v141, v125
	v_mfma_f32_32x32x16_bf16 a[0:15], v[44:47], v[156:159], a[0:15]
	v_add_f32_e32 v48, v48, v137
	v_add_f32_e32 v49, v49, v138
	v_add_f32_e32 v48, v48, v139
	v_exp_f32_e32 v142, v126
	v_exp_f32_e32 v143, v127
	v_exp_f32_e32 v144, v96
	v_mfma_f32_32x32x16_bf16 a[16:31], v[44:47], v[160:163], a[16:31]
	v_add_f32_e32 v44, v49, v140
	v_add_f32_e32 v45, v48, v141
	v_exp_f32_e32 v145, v97
	v_exp_f32_e32 v146, v98
	v_mfma_f32_32x32x16_bf16 a[32:47], v[40:43], v[156:159], a[32:47]
	v_add_f32_e32 v237, v44, v142
	v_add_f32_e32 v236, v45, v143
	v_add_f32_e32 v44, v201, v144
	v_exp_f32_e32 v147, v99
	v_exp_f32_e32 v148, v100
	v_exp_f32_e32 v149, v101
	v_mfma_f32_32x32x16_bf16 a[48:63], v[40:43], v[160:163], a[48:63]
	v_add_f32_e32 v40, v201, v145
	v_add_f32_e32 v41, v44, v146
	v_exp_f32_e32 v150, v102
	v_exp_f32_e32 v151, v103
	v_mfma_f32_32x32x16_bf16 a[64:79], v[36:39], v[156:159], a[64:79]
	v_add_f32_e32 v40, v40, v147
	v_add_f32_e32 v41, v41, v148
	v_add_f32_e32 v40, v40, v149
	v_exp_f32_e32 v152, v104
	v_exp_f32_e32 v153, v105
	v_exp_f32_e32 v154, v106
	v_mfma_f32_32x32x16_bf16 a[80:95], v[36:39], v[160:163], a[80:95]
	v_add_f32_e32 v36, v41, v150
	v_add_f32_e32 v37, v40, v151
	v_mfma_f32_32x32x16_bf16 a[96:111], v[32:35], v[156:159], a[96:111]
	v_exp_f32_e32 v155, v107
	v_exp_f32_e32 v156, v108
	v_add_f32_e32 v36, v36, v152
	v_add_f32_e32 v37, v37, v153
	v_add_f32_e32 v36, v36, v154
	v_exp_f32_e32 v157, v109
	v_exp_f32_e32 v158, v110
	v_exp_f32_e32 v159, v111
	v_mfma_f32_32x32x16_bf16 a[112:127], v[32:35], v[160:163], a[112:127]
	v_add_f32_e32 v32, v37, v155
	v_add_f32_e32 v33, v36, v156
	s_andn2_b64 vcc, exec, s[0:1]
	v_add_f32_e32 v32, v32, v157
	v_add_f32_e32 v238, v33, v158
	s_nop 0
	v_add_f32_e32 v239, v32, v159
	s_cbranch_vccz .LBB2_19
.LBB2_15:
	s_waitcnt lgkmcnt(0)
	v_exp_f32_e32 v80, v80
	v_exp_f32_e32 v81, v81
	v_mfma_f32_32x32x16_bf16 v[112:127], a[192:195], a[128:131], v[16:31]
	ds_read_b64_tr_b16 v[180:181], v208 offset:0
	v_cvt_pk_bf16_f32 v164, v128, v129
	v_exp_f32_e32 v82, v82
	v_exp_f32_e32 v83, v83
	v_mfma_f32_32x32x16_bf16 v[96:111], a[192:195], a[160:163], v[0:15]
	ds_read_b64_tr_b16 v[182:183], v208 offset:0x800
	v_cvt_pk_bf16_f32 v165, v130, v131
	v_mfma_f32_32x32x16_bf16 v[48:63], a[224:227], a[128:131], v[16:31]
	ds_read_b64_tr_b16 v[184:185], v208 offset:0x200
	v_exp_f32_e32 v240, v84
	v_exp_f32_e32 v241, v85
	v_cvt_pk_bf16_f32 v166, v132, v133
	v_mfma_f32_32x32x16_bf16 v[32:47], a[224:227], a[160:163], v[0:15]
	ds_read_b64_tr_b16 v[186:187], v208 offset:0xa00
	ds_read_b64_tr_b16 v[176:177], v208 offset:0x400
	v_exp_f32_e32 v242, v86
	v_exp_f32_e32 v243, v87
	v_cvt_pk_bf16_f32 v167, v134, v135
	v_exp_f32_e32 v198, v88
	v_exp_f32_e32 v199, v89
	v_mfma_f32_32x32x16_bf16 v[112:127], a[196:199], a[132:135], v[112:127]
	ds_read_b64_tr_b16 v[178:179], v208 offset:0xc00
	v_cvt_pk_bf16_f32 v128, v136, v137
	v_exp_f32_e32 v230, v90
	v_exp_f32_e32 v231, v91
	v_mfma_f32_32x32x16_bf16 v[96:111], a[196:199], a[164:167], v[96:111]
	ds_read_b64_tr_b16 v[188:189], v208 offset:0x600
	v_cvt_pk_bf16_f32 v129, v138, v139
	v_exp_f32_e32 v232, v92
	v_exp_f32_e32 v233, v93
	v_mfma_f32_32x32x16_bf16 v[48:63], a[228:231], a[132:135], v[48:63]
	ds_read_b64_tr_b16 v[190:191], v208 offset:0xe00
	v_cvt_pk_bf16_f32 v130, v140, v141
	v_mfma_f32_32x32x16_bf16 v[32:47], a[228:231], a[164:167], v[32:47]
	ds_read_b64_tr_b16 v[172:173], v208 offset:0x1000
	v_exp_f32_e32 v234, v94
	v_exp_f32_e32 v235, v95
	ds_read_b64_tr_b16 v[174:175], v208 offset:0x1800
	v_cvt_pk_bf16_f32 v131, v142, v143
	v_exp_f32_e32 v141, v64
	v_exp_f32_e32 v142, v65
	v_mfma_f32_32x32x16_bf16 v[112:127], a[200:203], a[136:139], v[112:127]
	ds_read_b64_tr_b16 v[168:169], v208 offset:0x1200
	v_cvt_pk_bf16_f32 v192, v144, v145
	v_exp_f32_e32 v143, v66
	v_mfma_f32_32x32x16_bf16 v[96:111], a[200:203], a[168:171], v[96:111]
	ds_read_b64_tr_b16 v[170:171], v208 offset:0x1a00
	v_exp_f32_e32 v244, v67
	v_cvt_pk_bf16_f32 v193, v146, v147
	v_mfma_f32_32x32x16_bf16 v[48:63], a[232:235], a[136:139], v[48:63]
	ds_read_b64_tr_b16 v[160:161], v208 offset:0x1400
	v_exp_f32_e32 v245, v68
	v_exp_f32_e32 v246, v69
	v_cvt_pk_bf16_f32 v194, v148, v149
	v_mfma_f32_32x32x16_bf16 v[32:47], a[232:235], a[168:171], v[32:47]
	ds_read_b64_tr_b16 v[162:163], v208 offset:0x1c00
	ds_read_b64_tr_b16 v[136:137], v208 offset:0x1600
	v_exp_f32_e32 v247, v70
	v_exp_f32_e32 v248, v71
	v_cvt_pk_bf16_f32 v195, v150, v151
	v_exp_f32_e32 v148, v72
	v_exp_f32_e32 v149, v73
	v_mfma_f32_32x32x16_bf16 v[112:127], a[204:207], a[140:143], v[112:127]
	ds_read_b64_tr_b16 v[138:139], v208 offset:0x1e00
	v_cvt_pk_bf16_f32 v144, v152, v153
	v_exp_f32_e32 v150, v74
	v_exp_f32_e32 v151, v75
	v_mfma_f32_32x32x16_bf16 v[96:111], a[204:207], a[172:175], v[96:111]
	ds_read_b64_tr_b16 v[132:133], v208 offset:0x2000
	v_cvt_pk_bf16_f32 v145, v154, v155
	v_exp_f32_e32 v152, v76
	v_exp_f32_e32 v153, v77
	v_mfma_f32_32x32x16_bf16 v[48:63], a[236:239], a[140:143], v[48:63]
	ds_read_b64_tr_b16 v[134:135], v208 offset:0x2800
	v_cvt_pk_bf16_f32 v146, v156, v157
	v_mfma_f32_32x32x16_bf16 v[32:47], a[236:239], a[172:175], v[32:47]
	ds_read_b64_tr_b16 v[92:93], v208 offset:0x2200
	v_exp_f32_e32 v154, v78
	v_exp_f32_e32 v155, v79
	ds_read_b64_tr_b16 v[94:95], v208 offset:0x2a00
	v_cvt_pk_bf16_f32 v147, v158, v159
	s_mov_b32 s0, s51
	v_mfma_f32_32x32x16_bf16 v[112:127], a[208:211], a[144:147], v[112:127]
	ds_read_b64_tr_b16 v[88:89], v208 offset:0x2400
	v_cvt_pk_bf16_f32 v84, v80, v81
	v_add_f32_e32 v64, v237, v80
	v_add_f32_e32 v65, v236, v81
	s_add_i32 s1, s17, 0xffffa000
	v_mfma_f32_32x32x16_bf16 v[96:111], a[208:211], a[176:179], v[96:111]
	ds_read_b64_tr_b16 v[90:91], v208 offset:0x2c00
	v_cvt_pk_bf16_f32 v85, v82, v83
	v_add_f32_e32 v64, v64, v82
	v_add_f32_e32 v65, v65, v83
	s_mov_b32 s81, s53
	v_mfma_f32_32x32x16_bf16 v[48:63], a[240:243], a[144:147], v[48:63]
	ds_read_b64_tr_b16 v[80:81], v208 offset:0x2600
	v_cvt_pk_bf16_f32 v86, v240, v241
	v_add_f32_e32 v64, v64, v240
	v_add_f32_e32 v65, v65, v241
	s_add_i32 s82, s17, 0xffffc000
	v_mfma_f32_32x32x16_bf16 v[32:47], a[240:243], a[176:179], v[32:47]
	ds_read_b64_tr_b16 v[82:83], v208 offset:0x2e00
	ds_read_b64_tr_b16 v[76:77], v208 offset:0x3000
	v_cvt_pk_bf16_f32 v87, v242, v243
	v_add_f32_e32 v64, v64, v242
	v_add_f32_e32 v65, v65, v243
	s_mov_b32 s83, s55
	v_mfma_f32_32x32x16_bf16 v[112:127], a[212:215], a[148:151], v[112:127]
	ds_read_b64_tr_b16 v[78:79], v208 offset:0x3800
	v_add_f32_e32 v64, v64, v198
	v_add_f32_e32 v65, v65, v199
	s_add_i32 s84, s17, 0xffffe000
	v_mfma_f32_32x32x16_bf16 v[96:111], a[212:215], a[180:183], v[96:111]
	ds_read_b64_tr_b16 v[72:73], v208 offset:0x3200
	v_add_f32_e32 v64, v64, v230
	v_add_f32_e32 v65, v65, v231
	s_mov_b32 s85, s57
	v_mfma_f32_32x32x16_bf16 v[48:63], a[244:247], a[148:151], v[48:63]
	ds_read_b64_tr_b16 v[74:75], v208 offset:0x3a00
	v_add_f32_e32 v64, v64, v232
	v_add_f32_e32 v65, v65, v233
	s_mov_b32 s86, s17
	v_mfma_f32_32x32x16_bf16 v[32:47], a[244:247], a[180:183], v[32:47]
	ds_read_b64_tr_b16 v[68:69], v208 offset:0x3400
	ds_read_b64_tr_b16 v[70:71], v208 offset:0x3c00
	v_add_f32_e32 v156, v64, v234
	v_add_f32_e32 v157, v65, v235
	s_mov_b32 s87, s31
	v_mfma_f32_32x32x16_bf16 v[112:127], a[216:219], a[152:155], v[112:127]
	ds_read_b64_tr_b16 v[64:65], v208 offset:0x3600
	v_cvt_pk_bf16_f32 v140, v141, v142
	v_add_f32_e32 v158, v238, v141
	v_add_f32_e32 v142, v239, v142
	v_mfma_f32_32x32x16_bf16 v[96:111], a[216:219], a[184:187], v[96:111]
	ds_read_b64_tr_b16 v[66:67], v208 offset:0x3e00
	v_cvt_pk_bf16_f32 v141, v143, v244
	v_add_f32_e32 v143, v158, v143
	v_add_f32_e32 v158, v142, v244
	v_mfma_f32_32x32x16_bf16 v[48:63], a[248:251], a[152:155], v[48:63]
	s_mov_b32 s88, s59
	v_cvt_pk_bf16_f32 v142, v245, v246
	v_add_f32_e32 v159, v143, v245
	v_add_f32_e32 v158, v158, v246
	v_mfma_f32_32x32x16_bf16 v[32:47], a[248:251], a[184:187], v[32:47]
	s_add_i32 s89, s17, 0xfffda080
	v_cvt_pk_bf16_f32 v143, v247, v248
	v_add_f32_e32 v159, v159, v247
	v_add_f32_e32 v158, v158, v248
	v_mfma_f32_32x32x16_bf16 v[112:127], a[220:223], a[156:159], v[112:127]
	s_mov_b32 s90, s61
	v_add_f32_e32 v159, v159, v148
	v_add_f32_e32 v158, v158, v149
	v_mfma_f32_32x32x16_bf16 v[96:111], a[220:223], a[188:191], v[96:111]
	v_add_f32_e32 v159, v159, v150
	v_add_f32_e32 v158, v158, v151
	v_mfma_f32_32x32x16_bf16 v[48:63], a[252:255], a[156:159], v[48:63]
	s_mov_b32 s91, s62
	v_add_f32_e32 v159, v159, v152
	v_add_f32_e32 v158, v158, v153
	v_mfma_f32_32x32x16_bf16 v[32:47], a[252:255], a[188:191], v[32:47]
	s_add_i32 s92, s17, 0xfffde080
	v_add_f32_e32 v159, v159, v154
	v_add_f32_e32 v158, v158, v155
	s_nop 4
	v_add_f32_e32 v156, v156, v157
	s_waitcnt vmcnt(0) lgkmcnt(0)
	s_barrier
	s_nop 0
	v_mov_b32_e32 v157, v156
	s_nop 1
	v_permlane32_swap_b32_e32 v156, v157
	v_add_f32_e32 v156, v156, v157
	v_add_f32_e32 v197, v197, v156
	v_add_f32_e32 v156, v159, v158
	v_mov_b32_e32 v157, v156
	s_nop 1
	v_permlane32_swap_b32_e32 v156, v157
	v_add_f32_e32 v156, v156, v157
	v_add_f32_e32 v196, v196, v156
	s_nop 1
	v_mfma_f32_32x32x16_bf16 a[0:15], v[180:183], v[164:167], a[0:15]
	s_mov_b32 m0, s0
	s_nop 0
	buffer_load_dwordx4 v209, s[4:7], s1 offen lds
	v_mfma_f32_32x32x16_bf16 a[16:31], v[180:183], v[192:195], a[16:31]
	s_mov_b32 m0, s81
	s_nop 0
	buffer_load_dwordx4 v210, s[4:7], s82 offen lds
	ds_read_b128 a[192:195], v204 offset:0
	v_mfma_f32_32x32x16_bf16 a[32:47], v[184:187], v[164:167], a[32:47]
	s_mov_b32 m0, s83
	s_nop 0
	buffer_load_dwordx4 v209, s[4:7], s84 offen lds
	ds_read_b128 a[196:199], v205 offset:0
	v_mfma_f32_32x32x16_bf16 a[48:63], v[184:187], v[192:195], a[48:63]
	s_mov_b32 m0, s85
	s_nop 0
	buffer_load_dwordx4 v210, s[4:7], s86 offen lds
	ds_read_b128 a[200:203], v206 offset:0
	v_mfma_f32_32x32x16_bf16 a[64:79], v[176:179], v[164:167], a[64:79]
	s_mov_b32 m0, s87
	s_nop 0
	buffer_load_dwordx4 v211, s[20:23], s19 offen lds
	ds_read_b128 a[204:207], v207 offset:0
	v_mfma_f32_32x32x16_bf16 a[80:95], v[176:179], v[192:195], a[80:95]
	s_mov_b32 m0, s88
	s_nop 0
	buffer_load_dwordx4 v211, s[20:23], s89 offen lds
	ds_read_b128 a[208:211], v204 offset:128
	v_mfma_f32_32x32x16_bf16 a[96:111], v[188:191], v[164:167], a[96:111]
	s_mov_b32 m0, s90
	s_nop 0
	buffer_load_dwordx4 v211, s[20:23], s24 offen lds
	ds_read_b128 a[212:215], v205 offset:128
	v_mfma_f32_32x32x16_bf16 a[112:127], v[188:191], v[192:195], a[112:127]
	s_mov_b32 m0, s91
	s_nop 0
	buffer_load_dwordx4 v211, s[20:23], s92 offen lds
	ds_read_b128 a[216:219], v206 offset:128
	v_mfma_f32_32x32x16_bf16 a[0:15], v[172:175], v[128:131], a[0:15]
	ds_read_b128 a[220:223], v207 offset:128
	v_max3_f32 v156, v112, v113, v48
	v_max3_f32 v157, v114, v115, v49
	v_max3_f32 v156, v156, v50, v51
	v_mfma_f32_32x32x16_bf16 a[16:31], v[172:175], v[144:147], a[16:31]
	ds_read_b128 a[224:227], v204 offset:8192
	v_max3_f32 v156, v156, v116, v117
	v_max3_f32 v157, v157, v118, v119
	v_max3_f32 v156, v156, v52, v53
	v_max3_f32 v157, v157, v54, v55
	v_mfma_f32_32x32x16_bf16 a[32:47], v[168:171], v[128:131], a[32:47]
	ds_read_b128 a[228:231], v205 offset:8192
	v_max3_f32 v156, v156, v120, v121
	v_max3_f32 v157, v157, v122, v123
	v_max3_f32 v156, v156, v56, v57
	v_max3_f32 v157, v157, v58, v59
	v_mfma_f32_32x32x16_bf16 a[48:63], v[168:171], v[144:147], a[48:63]
	ds_read_b128 a[232:235], v206 offset:8192
	v_max3_f32 v156, v156, v124, v125
	v_max3_f32 v157, v157, v126, v127
	v_max3_f32 v156, v156, v60, v61
	v_max3_f32 v157, v157, v62, v63
	v_mfma_f32_32x32x16_bf16 a[64:79], v[160:163], v[128:131], a[64:79]
	ds_read_b128 a[236:239], v207 offset:8192
	v_max3_f32 v158, v96, v97, v32
	v_max3_f32 v159, v98, v99, v33
	v_max3_f32 v158, v158, v34, v35
	v_mfma_f32_32x32x16_bf16 a[80:95], v[160:163], v[144:147], a[80:95]
	ds_read_b128 a[240:243], v204 offset:8320
	v_max3_f32 v158, v158, v100, v101
	v_max3_f32 v159, v159, v102, v103
	v_max3_f32 v158, v158, v36, v37
	v_max3_f32 v159, v159, v38, v39
	v_mfma_f32_32x32x16_bf16 a[96:111], v[136:139], v[128:131], a[96:111]
	ds_read_b128 a[244:247], v205 offset:8320
	v_max3_f32 v128, v158, v104, v105
	v_max3_f32 v129, v159, v106, v107
	v_max3_f32 v128, v128, v40, v41
	v_max3_f32 v129, v129, v42, v43
	v_mfma_f32_32x32x16_bf16 a[112:127], v[136:139], v[144:147], a[112:127]
	ds_read_b128 a[248:251], v206 offset:8320
	v_max3_f32 v128, v128, v108, v109
	v_max3_f32 v129, v129, v110, v111
	v_max3_f32 v128, v128, v44, v45
	v_max3_f32 v130, v129, v46, v47
	v_mfma_f32_32x32x16_bf16 a[0:15], v[132:135], v[84:87], a[0:15]
	ds_read_b128 a[252:255], v207 offset:8320
	v_max_f32_e32 v129, v156, v157
	v_mov_b32_e32 v131, v129
	s_nop 1
	v_permlane32_swap_b32_e32 v129, v131
	v_max_f32_e32 v129, v129, v131
	v_mfma_f32_32x32x16_bf16 a[16:31], v[132:135], v[140:143], a[16:31]
	v_max_f32_e32 v128, v128, v130
	v_mov_b32_e32 v130, v128
	s_nop 1
	v_permlane32_swap_b32_e32 v128, v130
	v_max_f32_e32 v128, v128, v130
	v_max_f32_e32 v130, v129, v129
	v_max_f32_e32 v131, v128, v128
	v_max_f32_e32 v130, v130, v131
	v_mfma_f32_32x32x16_bf16 a[32:47], v[92:95], v[84:87], a[32:47]
	v_cmp_lt_f32_e32 vcc, s79, v130
	s_cmp_lg_u64 vcc, 0
	s_cselect_b64 s[0:1], -1, 0
	s_cbranch_vccnz .LBB2_20
.LBB2_16:
	v_cvt_pk_bf16_f32 v156, v198, v199
	v_cvt_pk_bf16_f32 v157, v230, v231
	v_cvt_pk_bf16_f32 v158, v232, v233
	v_cvt_pk_bf16_f32 v159, v234, v235
	v_cvt_pk_bf16_f32 v160, v148, v149
	v_cvt_pk_bf16_f32 v161, v150, v151
	v_cvt_pk_bf16_f32 v162, v152, v153
	v_cvt_pk_bf16_f32 v163, v154, v155
	v_exp_f32_e32 v128, v112
	v_exp_f32_e32 v129, v113
	v_mfma_f32_32x32x16_bf16 a[48:63], v[92:95], v[140:143], a[48:63]
	v_exp_f32_e32 v130, v114
	v_exp_f32_e32 v131, v115
	v_mfma_f32_32x32x16_bf16 a[64:79], v[88:91], v[84:87], a[64:79]
	v_add_f32_e32 v92, v201, v128
	v_add_f32_e32 v93, v201, v129
	v_exp_f32_e32 v132, v116
	v_exp_f32_e32 v133, v117
	v_exp_f32_e32 v134, v118
	v_mfma_f32_32x32x16_bf16 a[80:95], v[88:91], v[140:143], a[80:95]
	v_add_f32_e32 v88, v92, v130
	v_add_f32_e32 v89, v93, v131
	v_exp_f32_e32 v135, v119
	v_exp_f32_e32 v136, v120
	v_mfma_f32_32x32x16_bf16 a[96:111], v[80:83], v[84:87], a[96:111]
	v_add_f32_e32 v84, v88, v132
	v_add_f32_e32 v85, v89, v133
	v_add_f32_e32 v84, v84, v134
	v_exp_f32_e32 v137, v121
	v_exp_f32_e32 v138, v122
	v_exp_f32_e32 v139, v123
	v_mfma_f32_32x32x16_bf16 a[112:127], v[80:83], v[140:143], a[112:127]
	v_add_f32_e32 v80, v85, v135
	v_add_f32_e32 v81, v84, v136
	v_exp_f32_e32 v140, v124
	v_exp_f32_e32 v141, v125
	v_mfma_f32_32x32x16_bf16 a[0:15], v[76:79], v[156:159], a[0:15]
	v_add_f32_e32 v80, v80, v137
	v_add_f32_e32 v81, v81, v138
	v_add_f32_e32 v80, v80, v139
	v_exp_f32_e32 v142, v126
	v_exp_f32_e32 v143, v127
	v_exp_f32_e32 v144, v96
	v_mfma_f32_32x32x16_bf16 a[16:31], v[76:79], v[160:163], a[16:31]
	v_add_f32_e32 v76, v81, v140
	v_add_f32_e32 v77, v80, v141
	v_exp_f32_e32 v145, v97
	v_exp_f32_e32 v146, v98
	v_mfma_f32_32x32x16_bf16 a[32:47], v[72:75], v[156:159], a[32:47]
	v_add_f32_e32 v239, v76, v142
	v_add_f32_e32 v238, v77, v143
	v_add_f32_e32 v76, v201, v144
	v_exp_f32_e32 v147, v99
	v_exp_f32_e32 v148, v100
	v_exp_f32_e32 v149, v101
	v_mfma_f32_32x32x16_bf16 a[48:63], v[72:75], v[160:163], a[48:63]
	v_add_f32_e32 v72, v201, v145
	v_add_f32_e32 v73, v76, v146
	v_exp_f32_e32 v150, v102
	v_exp_f32_e32 v151, v103
	v_mfma_f32_32x32x16_bf16 a[64:79], v[68:71], v[156:159], a[64:79]
	v_add_f32_e32 v72, v72, v147
	v_add_f32_e32 v73, v73, v148
	v_add_f32_e32 v72, v72, v149
	v_exp_f32_e32 v152, v104
	v_exp_f32_e32 v153, v105
	v_exp_f32_e32 v154, v106
	v_mfma_f32_32x32x16_bf16 a[80:95], v[68:71], v[160:163], a[80:95]
	v_add_f32_e32 v68, v73, v150
	v_add_f32_e32 v69, v72, v151
	v_mfma_f32_32x32x16_bf16 a[96:111], v[64:67], v[156:159], a[96:111]
	v_exp_f32_e32 v155, v107
	v_exp_f32_e32 v156, v108
	v_add_f32_e32 v68, v68, v152
	v_add_f32_e32 v69, v69, v153
	v_add_f32_e32 v68, v68, v154
	v_exp_f32_e32 v157, v109
	v_exp_f32_e32 v158, v110
	v_exp_f32_e32 v159, v111
	v_mfma_f32_32x32x16_bf16 a[112:127], v[64:67], v[160:163], a[112:127]
	v_add_f32_e32 v64, v69, v155
	v_add_f32_e32 v65, v68, v156
	s_andn2_b64 vcc, exec, s[0:1]
	v_add_f32_e32 v64, v64, v157
	v_add_f32_e32 v240, v65, v158
	s_nop 0
	v_add_f32_e32 v241, v64, v159
	s_cbranch_vccz .LBB2_21
